# fp8 MX MFMAs with unit scales issued without the ld_scale half (same fp8 e4m3 16x16x128 op, scale 2^0)
# speedup vs baseline: 1.0089x; 1.0089x over previous
.LBB0_1025:
	ds_read_b128 v[140:143], v134
	ds_read_b128 v[144:147], v134 offset:1024
	ds_read_b128 v[148:151], v134 offset:2048
	ds_read_b128 v[152:155], v134 offset:3072
	ds_read_b128 v[156:159], v135
	ds_read_b128 v[160:163], v135 offset:1024
	ds_read_b128 v[164:167], v135 offset:2048
	ds_read_b128 v[168:171], v135 offset:3072
	s_add_i32 s13, s12, 0xfffc0080
	s_cmp_eq_u32 s1, 12
	s_cselect_b32 s45, s29, s41
	s_cselect_b32 s44, s28, s40
	s_cselect_b32 s47, s31, s43
	s_cselect_b32 s46, s30, s42
	s_cselect_b32 s13, 0, s13
	s_cselect_b32 s49, s35, s53
	s_cselect_b32 s48, s34, s52
	s_cselect_b32 s51, s63, s5
	s_cselect_b32 s50, s62, s4
	s_mov_b32 m0, s91
	ds_read_b128 v[198:201], v136
	ds_read_b128 v[202:205], v136 offset:1024
	ds_read_b128 v[206:209], v136 offset:2048
	ds_read_b128 v[210:213], v136 offset:3072
	ds_read_b128 v[214:217], v136 offset:4096
	ds_read_b128 v[218:221], v136 offset:5120
	ds_read_b128 v[222:225], v136 offset:6144
	ds_read_b128 v[226:229], v136 offset:7168
	buffer_load_dwordx4 v132, s[40:43], s12 offen lds
	s_mov_b32 m0, s92
	s_nop 0
	buffer_load_dwordx4 v133, s[40:43], s12 offen lds
	s_waitcnt vmcnt(8)
	s_waitcnt lgkmcnt(0)
	s_barrier
	s_setprio 1
	s_waitcnt lgkmcnt(6)
	v_mfma_f32_16x16x128_f8f6f4 v[124:127], v[140:147], v[198:205], v[124:127]
	v_mfma_f32_16x16x128_f8f6f4 v[120:123], v[148:155], v[198:205], v[120:123]
	s_waitcnt lgkmcnt(4)
	v_mfma_f32_16x16x128_f8f6f4 v[108:111], v[140:147], v[206:213], v[108:111]
	v_mfma_f32_16x16x128_f8f6f4 v[104:107], v[148:155], v[206:213], v[104:107]
	s_waitcnt lgkmcnt(2)
	v_mfma_f32_16x16x128_f8f6f4 v[172:175], v[140:147], v[214:221], v[92:95]
	v_mfma_f32_16x16x128_f8f6f4 v[246:249], v[148:155], v[214:221], v[88:91]
	s_waitcnt lgkmcnt(0)
	v_mfma_f32_16x16x128_f8f6f4 v[250:253], v[140:147], v[222:229], v[76:79]
	v_mfma_f32_16x16x128_f8f6f4 v[194:197], v[148:155], v[222:229], v[72:75]
	s_setprio 0
	s_setprio 1
	v_mfma_f32_16x16x128_f8f6f4 v[116:119], v[156:163], v[198:205], v[116:119]
	v_mfma_f32_16x16x128_f8f6f4 v[112:115], v[164:171], v[198:205], v[112:115]
	v_mfma_f32_16x16x128_f8f6f4 v[100:103], v[156:163], v[206:213], v[100:103]
	v_mfma_f32_16x16x128_f8f6f4 v[96:99], v[164:171], v[206:213], v[96:99]
	v_mfma_f32_16x16x128_f8f6f4 v[198:201], v[156:163], v[214:221], v[84:87]
	v_mfma_f32_16x16x128_f8f6f4 v[202:205], v[164:171], v[214:221], v[80:83]
	v_mfma_f32_16x16x128_f8f6f4 v[206:209], v[156:163], v[222:229], v[68:71]
	v_mfma_f32_16x16x128_f8f6f4 v[210:213], v[164:171], v[222:229], v[64:67]
	s_setprio 0
	s_barrier
	s_mov_b32 m0, s69
	s_nop 3
	ds_read_b128 v[64:67], v136 offset:16384
	ds_read_b128 v[68:71], v136 offset:17408
	ds_read_b128 v[72:75], v136 offset:18432
	ds_read_b128 v[76:79], v136 offset:19456
	ds_read_b128 v[80:83], v136 offset:20480
	ds_read_b128 v[84:87], v136 offset:21504
	ds_read_b128 v[88:91], v136 offset:22528
	ds_read_b128 v[92:95], v136 offset:23552
	buffer_load_dwordx4 v245, s[48:51], s13 offen lds
	s_mov_b32 m0, s70
	s_add_i32 s21, s13, 0x40000
	buffer_load_dwordx4 v244, s[48:51], s13 offen lds
	s_mov_b32 m0, s71
	s_nop 0
	buffer_load_dwordx4 v245, s[48:51], s21 offen lds
	s_mov_b32 m0, s72
	s_nop 0
	buffer_load_dwordx4 v244, s[48:51], s21 offen lds
	s_mov_b32 m0, s68
	s_nop 0
	buffer_load_dwordx4 v132, s[44:47], s13 offen lds
	s_mov_b32 m0, s73
	s_nop 0
	buffer_load_dwordx4 v133, s[44:47], s13 offen lds
	s_waitcnt vmcnt(8)
	s_waitcnt lgkmcnt(0)
	s_barrier
	s_setprio 1
	s_waitcnt lgkmcnt(6)
	v_mfma_f32_16x16x128_f8f6f4 v[60:63], v[140:147], v[64:71], v[60:63]
	s_waitcnt lgkmcnt(0)
	v_mfma_f32_16x16x128_f8f6f4 v[16:19], v[140:147], v[88:95], v[16:19]
	v_mfma_f32_16x16x128_f8f6f4 v[214:217], v[148:155], v[64:71], v[12:15]
	v_mfma_f32_16x16x128_f8f6f4 v[218:221], v[140:147], v[72:79], v[48:51]
	v_mfma_f32_16x16x128_f8f6f4 v[222:225], v[148:155], v[72:79], v[44:47]
	v_mfma_f32_16x16x128_f8f6f4 v[226:229], v[140:147], v[80:87], v[32:35]
	v_mfma_f32_16x16x128_f8f6f4 v[178:181], v[148:155], v[80:87], v[28:31]
	v_mfma_f32_16x16x128_f8f6f4 v[182:185], v[148:155], v[88:95], v[8:11]
	s_setprio 0
	s_setprio 1
	v_mfma_f32_16x16x128_f8f6f4 v[56:59], v[156:163], v[64:71], v[56:59]
	v_mfma_f32_16x16x128_f8f6f4 v[52:55], v[164:171], v[64:71], v[52:55]
	v_mfma_f32_16x16x128_f8f6f4 v[186:189], v[156:163], v[72:79], v[40:43]
	v_mfma_f32_16x16x128_f8f6f4 v[190:193], v[164:171], v[72:79], v[36:39]
	v_mfma_f32_16x16x128_f8f6f4 v[236:239], v[156:163], v[80:87], v[24:27]
	v_mfma_f32_16x16x128_f8f6f4 v[240:243], v[164:171], v[80:87], v[20:23]
	v_mfma_f32_16x16x128_f8f6f4 v[232:235], v[156:163], v[88:95], v[4:7]
	v_mfma_f32_16x16x128_f8f6f4 v[128:131], v[164:171], v[88:95], v[0:3]
	s_setprio 0
	s_barrier
	s_nop 4
	ds_read_b128 v[0:3], v137
	ds_read_b128 v[4:7], v137 offset:1024
	ds_read_b128 v[20:23], v137 offset:2048
	ds_read_b128 v[24:27], v137 offset:3072
	ds_read_b128 v[140:143], v138
	ds_read_b128 v[144:147], v138 offset:1024
	ds_read_b128 v[148:151], v138 offset:2048
	ds_read_b128 v[152:155], v138 offset:3072
	s_mov_b32 m0, s76
	ds_read_b128 v[8:11], v136 offset:32768
	ds_read_b128 v[12:15], v136 offset:33792
	ds_read_b128 v[28:31], v136 offset:34816
	ds_read_b128 v[32:35], v136 offset:35840
	ds_read_b128 v[36:39], v136 offset:36864
	ds_read_b128 v[40:43], v136 offset:37888
	ds_read_b128 v[44:47], v136 offset:38912
	ds_read_b128 v[48:51], v136 offset:39936
	buffer_load_dwordx4 v132, s[44:47], s21 offen lds
	s_mov_b32 m0, s77
	s_nop 0
	buffer_load_dwordx4 v133, s[44:47], s21 offen lds
	s_waitcnt vmcnt(8)
	s_waitcnt lgkmcnt(0)
	s_barrier
	s_setprio 1
	s_waitcnt lgkmcnt(6)
	v_mfma_f32_16x16x128_f8f6f4 v[124:127], v[0:7], v[8:15], v[124:127]
	v_mfma_f32_16x16x128_f8f6f4 v[120:123], v[20:27], v[8:15], v[120:123]
	s_waitcnt lgkmcnt(4)
	v_mfma_f32_16x16x128_f8f6f4 v[108:111], v[0:7], v[28:35], v[108:111]
	v_mfma_f32_16x16x128_f8f6f4 v[104:107], v[20:27], v[28:35], v[104:107]
	s_waitcnt lgkmcnt(2)
	v_mfma_f32_16x16x128_f8f6f4 v[92:95], v[0:7], v[36:43], v[172:175]
	v_mfma_f32_16x16x128_f8f6f4 v[88:91], v[20:27], v[36:43], v[246:249]
	s_waitcnt lgkmcnt(0)
	v_mfma_f32_16x16x128_f8f6f4 v[76:79], v[0:7], v[44:51], v[250:253]
	v_mfma_f32_16x16x128_f8f6f4 v[72:75], v[20:27], v[44:51], v[194:197]
	s_setprio 0
	s_setprio 1
	v_mfma_f32_16x16x128_f8f6f4 v[116:119], v[140:147], v[8:15], v[116:119]
	v_mfma_f32_16x16x128_f8f6f4 v[112:115], v[148:155], v[8:15], v[112:115]
	v_mfma_f32_16x16x128_f8f6f4 v[100:103], v[140:147], v[28:35], v[100:103]
	v_mfma_f32_16x16x128_f8f6f4 v[96:99], v[148:155], v[28:35], v[96:99]
	v_mfma_f32_16x16x128_f8f6f4 v[84:87], v[140:147], v[36:43], v[198:201]
	v_mfma_f32_16x16x128_f8f6f4 v[80:83], v[148:155], v[36:43], v[202:205]
	v_mfma_f32_16x16x128_f8f6f4 v[68:71], v[140:147], v[44:51], v[206:209]
	v_mfma_f32_16x16x128_f8f6f4 v[64:67], v[148:155], v[44:51], v[210:213]
	s_setprio 0
	s_barrier
	s_mov_b32 m0, s78
	s_or_b32 s21, s13, 0x80
	ds_read_b128 v[36:39], v136 offset:49152
	ds_read_b128 v[40:43], v136 offset:50176
	ds_read_b128 v[156:159], v136 offset:51200
	ds_read_b128 v[160:163], v136 offset:52224
	ds_read_b128 v[164:167], v136 offset:53248
	ds_read_b128 v[168:171], v136 offset:54272
	ds_read_b128 v[198:201], v136 offset:55296
	ds_read_b128 v[202:205], v136 offset:56320
	buffer_load_dwordx4 v245, s[48:51], s21 offen lds
	s_mov_b32 m0, s79
	s_add_i32 s13, s13, 0x40080
	buffer_load_dwordx4 v244, s[48:51], s21 offen lds
	s_mov_b32 m0, s83
	s_nop 0
	buffer_load_dwordx4 v245, s[48:51], s13 offen lds
	s_mov_b32 m0, s88
	s_nop 0
	buffer_load_dwordx4 v244, s[48:51], s13 offen lds
	s_mov_b32 m0, s80
	s_nop 0
	buffer_load_dwordx4 v132, s[44:47], s21 offen lds
	s_mov_b32 m0, s82
	s_nop 0
	buffer_load_dwordx4 v133, s[44:47], s21 offen lds
	s_waitcnt vmcnt(8)
	s_waitcnt lgkmcnt(0)
	s_barrier
	s_setprio 1
	s_waitcnt lgkmcnt(6)
	v_mfma_f32_16x16x128_f8f6f4 v[60:63], v[0:7], v[36:43], v[60:63]
	v_mfma_f32_16x16x128_f8f6f4 v[12:15], v[20:27], v[36:43], v[214:217]
	s_waitcnt lgkmcnt(4)
	v_mfma_f32_16x16x128_f8f6f4 v[48:51], v[0:7], v[156:163], v[218:221]
	v_mfma_f32_16x16x128_f8f6f4 v[44:47], v[20:27], v[156:163], v[222:225]
	s_waitcnt lgkmcnt(2)
	v_mfma_f32_16x16x128_f8f6f4 v[32:35], v[0:7], v[164:171], v[226:229]
	v_mfma_f32_16x16x128_f8f6f4 v[28:31], v[20:27], v[164:171], v[178:181]
	s_waitcnt lgkmcnt(0)
	v_mfma_f32_16x16x128_f8f6f4 v[16:19], v[0:7], v[198:205], v[16:19]
	v_mfma_f32_16x16x128_f8f6f4 v[8:11], v[20:27], v[198:205], v[182:185]
	s_setprio 0
	s_setprio 1
	v_mfma_f32_16x16x128_f8f6f4 v[56:59], v[140:147], v[36:43], v[56:59]
	v_mfma_f32_16x16x128_f8f6f4 v[52:55], v[148:155], v[36:43], v[52:55]
	v_mfma_f32_16x16x128_f8f6f4 v[40:43], v[140:147], v[156:163], v[186:189]
	v_mfma_f32_16x16x128_f8f6f4 v[36:39], v[148:155], v[156:163], v[190:193]
	v_mfma_f32_16x16x128_f8f6f4 v[24:27], v[140:147], v[164:171], v[236:239]
	v_mfma_f32_16x16x128_f8f6f4 v[20:23], v[148:155], v[164:171], v[240:243]
	v_mfma_f32_16x16x128_f8f6f4 v[4:7], v[140:147], v[198:205], v[232:235]
	v_mfma_f32_16x16x128_f8f6f4 v[0:3], v[148:155], v[198:205], v[128:131]
	s_setprio 0
	s_barrier
	s_add_i32 s1, s1, 2
	s_addk_i32 s12, 0x100
	s_cmp_gt_u32 s1, 13
	s_cbranch_scc0 .LBB0_1025
	s_and_b64 vcc, exec, s[18:19]
	s_cbranch_vccz .LBB0_1028
	s_barrier

.LBB0_1051:
	v_add_u32_e32 v140, 0x10000, v150
	v_add_u32_e32 v144, 0x14000, v150
	ds_read_b128 v[120:123], v140
	ds_read_b128 v[124:127], v140 offset:1024
	ds_read_b128 v[136:139], v140 offset:2048
	ds_read_b128 v[140:143], v140 offset:3072
	ds_read_b128 v[152:155], v144
	ds_read_b128 v[156:159], v144 offset:1024
	ds_read_b128 v[160:163], v144 offset:2048
	ds_read_b128 v[164:167], v144 offset:3072
	s_add_i32 s38, s31, 0xfffc0080
	s_cmp_eq_u32 s29, 12
	s_cselect_b32 s45, s35, s41
	s_cselect_b32 s44, s34, s40
	s_cselect_b32 s47, s9, s43
	s_cselect_b32 s46, s8, s42
	s_cselect_b32 s38, 0, s38
	s_cselect_b32 s49, s3, s53
	s_cselect_b32 s48, s2, s52
	s_cselect_b32 s51, s13, s1
	s_cselect_b32 s50, s12, s0
	s_mov_b32 m0, s89
	ds_read_b128 v[168:171], v151
	ds_read_b128 v[172:175], v151 offset:1024
	ds_read_b128 v[198:201], v151 offset:2048
	ds_read_b128 v[202:205], v151 offset:3072
	ds_read_b128 v[206:209], v151 offset:4096
	ds_read_b128 v[210:213], v151 offset:5120
	ds_read_b128 v[214:217], v151 offset:6144
	ds_read_b128 v[218:221], v151 offset:7168
	buffer_load_dwordx4 v148, s[40:43], s31 offen lds
	s_mov_b32 m0, s88
	s_nop 0
	buffer_load_dwordx4 v149, s[40:43], s31 offen lds
	s_waitcnt vmcnt(8)
	s_waitcnt lgkmcnt(0)
	s_barrier
	s_setprio 1
	s_waitcnt lgkmcnt(6)
	v_mfma_f32_16x16x128_f8f6f4 v[132:135], v[120:127], v[168:175], v[132:135]
	v_mfma_f32_16x16x128_f8f6f4 v[128:131], v[136:143], v[168:175], v[128:131]
	s_waitcnt lgkmcnt(4)
	v_mfma_f32_16x16x128_f8f6f4 v[108:111], v[120:127], v[198:205], v[108:111]
	v_mfma_f32_16x16x128_f8f6f4 v[104:107], v[136:143], v[198:205], v[104:107]
	s_waitcnt lgkmcnt(2)
	v_mfma_f32_16x16x128_f8f6f4 v[178:181], v[120:127], v[206:213], v[92:95]
	v_mfma_f32_16x16x128_f8f6f4 v[182:185], v[136:143], v[206:213], v[88:91]
	s_waitcnt lgkmcnt(0)
	v_mfma_f32_16x16x128_f8f6f4 v[186:189], v[120:127], v[214:221], v[76:79]
	v_mfma_f32_16x16x128_f8f6f4 v[190:193], v[136:143], v[214:221], v[72:75]
	s_setprio 0
	s_setprio 1
	v_mfma_f32_16x16x128_f8f6f4 v[116:119], v[152:159], v[168:175], v[116:119]
	v_mfma_f32_16x16x128_f8f6f4 v[112:115], v[160:167], v[168:175], v[112:115]
	v_mfma_f32_16x16x128_f8f6f4 v[100:103], v[152:159], v[198:205], v[100:103]
	v_mfma_f32_16x16x128_f8f6f4 v[96:99], v[160:167], v[198:205], v[96:99]
	v_mfma_f32_16x16x128_f8f6f4 v[168:171], v[152:159], v[206:213], v[84:87]
	v_mfma_f32_16x16x128_f8f6f4 v[172:175], v[160:167], v[206:213], v[80:83]
	v_mfma_f32_16x16x128_f8f6f4 v[194:197], v[152:159], v[214:221], v[68:71]
	v_mfma_f32_16x16x128_f8f6f4 v[198:201], v[160:167], v[214:221], v[64:67]
	s_setprio 0
	s_barrier
	s_mov_b32 m0, s77
	s_nop 3
	ds_read_b128 v[64:67], v151 offset:16384
	ds_read_b128 v[68:71], v151 offset:17408
	ds_read_b128 v[72:75], v151 offset:18432
	ds_read_b128 v[76:79], v151 offset:19456
	ds_read_b128 v[80:83], v151 offset:20480
	ds_read_b128 v[84:87], v151 offset:21504
	ds_read_b128 v[88:91], v151 offset:22528
	ds_read_b128 v[92:95], v151 offset:23552
	buffer_load_dwordx4 v146, s[48:51], s38 offen lds
	s_mov_b32 m0, s64
	s_add_i32 s39, s38, 0x40000
	buffer_load_dwordx4 v147, s[48:51], s38 offen lds
	s_mov_b32 m0, s65
	s_nop 0
	buffer_load_dwordx4 v146, s[48:51], s39 offen lds
	s_mov_b32 m0, s22
	s_nop 0
	buffer_load_dwordx4 v147, s[48:51], s39 offen lds
	s_mov_b32 m0, s92
	s_nop 0
	buffer_load_dwordx4 v148, s[44:47], s38 offen lds
	s_mov_b32 m0, s23
	s_nop 0
	buffer_load_dwordx4 v149, s[44:47], s38 offen lds
	s_waitcnt vmcnt(8)
	s_waitcnt lgkmcnt(0)
	s_barrier
	s_setprio 1
	s_waitcnt lgkmcnt(6)
	v_mfma_f32_16x16x128_f8f6f4 v[60:63], v[120:127], v[64:71], v[60:63]
	v_mfma_f32_16x16x128_f8f6f4 v[16:19], v[136:143], v[64:71], v[16:19]
	s_waitcnt lgkmcnt(4)
	v_mfma_f32_16x16x128_f8f6f4 v[202:205], v[120:127], v[72:79], v[48:51]
	v_mfma_f32_16x16x128_f8f6f4 v[206:209], v[136:143], v[72:79], v[44:47]
	s_waitcnt lgkmcnt(2)
	v_mfma_f32_16x16x128_f8f6f4 v[210:213], v[120:127], v[80:87], v[32:35]
	v_mfma_f32_16x16x128_f8f6f4 v[214:217], v[136:143], v[80:87], v[28:31]
	s_waitcnt lgkmcnt(0)
	v_mfma_f32_16x16x128_f8f6f4 v[218:221], v[120:127], v[88:95], v[12:15]
	v_mfma_f32_16x16x128_f8f6f4 v[222:225], v[136:143], v[88:95], v[8:11]
	s_setprio 0
	s_setprio 1
	v_mfma_f32_16x16x128_f8f6f4 v[56:59], v[152:159], v[64:71], v[56:59]
	v_mfma_f32_16x16x128_f8f6f4 v[52:55], v[160:167], v[64:71], v[52:55]
	v_mfma_f32_16x16x128_f8f6f4 v[226:229], v[152:159], v[72:79], v[40:43]
	v_mfma_f32_16x16x128_f8f6f4 v[232:235], v[160:167], v[72:79], v[36:39]
	v_mfma_f32_16x16x128_f8f6f4 v[236:239], v[152:159], v[80:87], v[24:27]
	v_mfma_f32_16x16x128_f8f6f4 v[240:243], v[160:167], v[80:87], v[20:23]
	v_mfma_f32_16x16x128_f8f6f4 v[244:247], v[152:159], v[88:95], v[4:7]
	v_mfma_f32_16x16x128_f8f6f4 v[248:251], v[160:167], v[88:95], v[0:3]
	s_setprio 0
	s_barrier
	v_add_u32_e32 v8, 0x18000, v150
	s_nop 3
	ds_read_b128 v[0:3], v8
	ds_read_b128 v[4:7], v8 offset:1024
	ds_read_b128 v[20:23], v8 offset:2048
	ds_read_b128 v[24:27], v8 offset:3072
	v_add_u32_e32 v8, 0x1c000, v150
	ds_read_b128 v[120:123], v8
	ds_read_b128 v[124:127], v8 offset:1024
	ds_read_b128 v[136:139], v8 offset:2048
	ds_read_b128 v[140:143], v8 offset:3072
	s_mov_b32 m0, s33
	ds_read_b128 v[8:11], v151 offset:32768
	ds_read_b128 v[12:15], v151 offset:33792
	ds_read_b128 v[28:31], v151 offset:34816
	ds_read_b128 v[32:35], v151 offset:35840
	ds_read_b128 v[36:39], v151 offset:36864
	ds_read_b128 v[40:43], v151 offset:37888
	ds_read_b128 v[44:47], v151 offset:38912
	ds_read_b128 v[48:51], v151 offset:39936
	buffer_load_dwordx4 v148, s[44:47], s39 offen lds
	s_mov_b32 m0, s96
	s_nop 0
	buffer_load_dwordx4 v149, s[44:47], s39 offen lds
	s_waitcnt vmcnt(8)
	s_waitcnt lgkmcnt(0)
	s_barrier
	s_setprio 1
	s_waitcnt lgkmcnt(6)
	v_mfma_f32_16x16x128_f8f6f4 v[132:135], v[0:7], v[8:15], v[132:135]
	v_mfma_f32_16x16x128_f8f6f4 v[128:131], v[20:27], v[8:15], v[128:131]
	s_waitcnt lgkmcnt(4)
	v_mfma_f32_16x16x128_f8f6f4 v[108:111], v[0:7], v[28:35], v[108:111]
	v_mfma_f32_16x16x128_f8f6f4 v[104:107], v[20:27], v[28:35], v[104:107]
	s_waitcnt lgkmcnt(2)
	v_mfma_f32_16x16x128_f8f6f4 v[92:95], v[0:7], v[36:43], v[178:181]
	v_mfma_f32_16x16x128_f8f6f4 v[88:91], v[20:27], v[36:43], v[182:185]
	s_waitcnt lgkmcnt(0)
	v_mfma_f32_16x16x128_f8f6f4 v[76:79], v[0:7], v[44:51], v[186:189]
	v_mfma_f32_16x16x128_f8f6f4 v[72:75], v[20:27], v[44:51], v[190:193]
	s_setprio 0
	s_setprio 1
	v_mfma_f32_16x16x128_f8f6f4 v[116:119], v[120:127], v[8:15], v[116:119]
	v_mfma_f32_16x16x128_f8f6f4 v[112:115], v[136:143], v[8:15], v[112:115]
	v_mfma_f32_16x16x128_f8f6f4 v[100:103], v[120:127], v[28:35], v[100:103]
	v_mfma_f32_16x16x128_f8f6f4 v[96:99], v[136:143], v[28:35], v[96:99]
	v_mfma_f32_16x16x128_f8f6f4 v[84:87], v[120:127], v[36:43], v[168:171]
	v_mfma_f32_16x16x128_f8f6f4 v[80:83], v[136:143], v[36:43], v[172:175]
	v_mfma_f32_16x16x128_f8f6f4 v[68:71], v[120:127], v[44:51], v[194:197]
	v_mfma_f32_16x16x128_f8f6f4 v[64:67], v[136:143], v[44:51], v[198:201]
	s_setprio 0
	s_barrier
	s_mov_b32 m0, s69
	s_or_b32 s39, s38, 0x80
	ds_read_b128 v[36:39], v151 offset:49152
	ds_read_b128 v[40:43], v151 offset:50176
	ds_read_b128 v[152:155], v151 offset:51200
	ds_read_b128 v[156:159], v151 offset:52224
	ds_read_b128 v[160:163], v151 offset:53248
	ds_read_b128 v[164:167], v151 offset:54272
	ds_read_b128 v[168:171], v151 offset:55296
	ds_read_b128 v[172:175], v151 offset:56320
	buffer_load_dwordx4 v146, s[48:51], s39 offen lds
	s_mov_b32 m0, s61
	s_add_i32 s38, s38, 0x40080
	buffer_load_dwordx4 v147, s[48:51], s39 offen lds
	s_mov_b32 m0, s83
	s_nop 0
	buffer_load_dwordx4 v146, s[48:51], s38 offen lds
	s_mov_b32 m0, s82
	s_nop 0
	buffer_load_dwordx4 v147, s[48:51], s38 offen lds
	s_mov_b32 m0, s71
	s_nop 0
	buffer_load_dwordx4 v148, s[44:47], s39 offen lds
	s_mov_b32 m0, s70
	s_nop 0
	buffer_load_dwordx4 v149, s[44:47], s39 offen lds
	s_waitcnt vmcnt(8)
	s_waitcnt lgkmcnt(0)
	s_barrier
	s_setprio 1
	s_waitcnt lgkmcnt(6)
	v_mfma_f32_16x16x128_f8f6f4 v[60:63], v[0:7], v[36:43], v[60:63]
	v_mfma_f32_16x16x128_f8f6f4 v[16:19], v[20:27], v[36:43], v[16:19]
	s_waitcnt lgkmcnt(4)
	v_mfma_f32_16x16x128_f8f6f4 v[48:51], v[0:7], v[152:159], v[202:205]
	v_mfma_f32_16x16x128_f8f6f4 v[44:47], v[20:27], v[152:159], v[206:209]
	s_waitcnt lgkmcnt(2)
	v_mfma_f32_16x16x128_f8f6f4 v[32:35], v[0:7], v[160:167], v[210:213]
	v_mfma_f32_16x16x128_f8f6f4 v[28:31], v[20:27], v[160:167], v[214:217]
	s_waitcnt lgkmcnt(0)
	v_mfma_f32_16x16x128_f8f6f4 v[12:15], v[0:7], v[168:175], v[218:221]
	v_mfma_f32_16x16x128_f8f6f4 v[8:11], v[20:27], v[168:175], v[222:225]
	s_setprio 0
	s_setprio 1
	v_mfma_f32_16x16x128_f8f6f4 v[56:59], v[120:127], v[36:43], v[56:59]
	v_mfma_f32_16x16x128_f8f6f4 v[52:55], v[136:143], v[36:43], v[52:55]
	v_mfma_f32_16x16x128_f8f6f4 v[40:43], v[120:127], v[152:159], v[226:229]
	v_mfma_f32_16x16x128_f8f6f4 v[36:39], v[136:143], v[152:159], v[232:235]
	v_mfma_f32_16x16x128_f8f6f4 v[24:27], v[120:127], v[160:167], v[236:239]
	v_mfma_f32_16x16x128_f8f6f4 v[20:23], v[136:143], v[160:167], v[240:243]
	v_mfma_f32_16x16x128_f8f6f4 v[4:7], v[120:127], v[168:175], v[244:247]
	v_mfma_f32_16x16x128_f8f6f4 v[0:3], v[136:143], v[168:175], v[248:251]
	s_setprio 0
	s_barrier
	s_add_i32 s29, s29, 2
	s_addk_i32 s31, 0x100
	s_cmp_gt_u32 s29, 13
	s_cbranch_scc0 .LBB0_1051
	s_and_b64 vcc, exec, s[62:63]
	s_cbranch_vccz .LBB0_1054
	s_barrier

.LBB0_1187:
	v_add_u32_e32 v140, 0x10000, v148
	v_add_u32_e32 v162, 0x14000, v148
	ds_read_b128 v[128:131], v140
	ds_read_b128 v[132:135], v140 offset:1024
	ds_read_b128 v[136:139], v140 offset:2048
	ds_read_b128 v[140:143], v140 offset:3072
	ds_read_b128 v[150:153], v162
	ds_read_b128 v[154:157], v162 offset:1024
	ds_read_b128 v[158:161], v162 offset:2048
	ds_read_b128 v[162:165], v162 offset:3072
	s_add_i32 s19, s13, 0xfffc0080
	s_cmp_eq_u32 s12, 12
	s_cselect_b32 s45, s23, s41
	s_cselect_b32 s44, s22, s40
	s_cselect_b32 s47, s29, s43
	s_cselect_b32 s46, s28, s42
	s_cselect_b32 s19, 0, s19
	s_cselect_b32 s49, s31, s53
	s_cselect_b32 s48, s30, s52
	s_cselect_b32 s51, s35, s5
	s_cselect_b32 s50, s34, s4
	s_mov_b32 m0, s83
	ds_read_b128 v[166:169], v149
	ds_read_b128 v[170:173], v149 offset:1024
	ds_read_b128 v[198:201], v149 offset:2048
	ds_read_b128 v[202:205], v149 offset:3072
	ds_read_b128 v[206:209], v149 offset:4096
	ds_read_b128 v[210:213], v149 offset:5120
	ds_read_b128 v[214:217], v149 offset:6144
	ds_read_b128 v[218:221], v149 offset:7168
	buffer_load_dwordx4 v146, s[40:43], s13 offen lds
	s_mov_b32 m0, s91
	s_nop 0
	buffer_load_dwordx4 v147, s[40:43], s13 offen lds
	s_waitcnt vmcnt(8)
	s_waitcnt lgkmcnt(0)
	s_barrier
	s_setprio 1
	s_waitcnt lgkmcnt(6)
	v_mfma_f32_16x16x128_f8f6f4 v[124:127], v[128:135], v[166:173], v[124:127]
	v_mfma_f32_16x16x128_f8f6f4 v[120:123], v[136:143], v[166:173], v[120:123]
	s_waitcnt lgkmcnt(4)
	v_mfma_f32_16x16x128_f8f6f4 v[108:111], v[128:135], v[198:205], v[108:111]
	v_mfma_f32_16x16x128_f8f6f4 v[104:107], v[136:143], v[198:205], v[104:107]
	s_waitcnt lgkmcnt(2)
	v_mfma_f32_16x16x128_f8f6f4 v[178:181], v[128:135], v[206:213], v[92:95]
	v_mfma_f32_16x16x128_f8f6f4 v[182:185], v[136:143], v[206:213], v[88:91]
	s_waitcnt lgkmcnt(0)
	v_mfma_f32_16x16x128_f8f6f4 v[186:189], v[128:135], v[214:221], v[76:79]
	v_mfma_f32_16x16x128_f8f6f4 v[190:193], v[136:143], v[214:221], v[72:75]
	s_setprio 0
	s_setprio 1
	v_mfma_f32_16x16x128_f8f6f4 v[116:119], v[150:157], v[166:173], v[116:119]
	v_mfma_f32_16x16x128_f8f6f4 v[112:115], v[158:165], v[166:173], v[112:115]
	v_mfma_f32_16x16x128_f8f6f4 v[100:103], v[150:157], v[198:205], v[100:103]
	v_mfma_f32_16x16x128_f8f6f4 v[96:99], v[158:165], v[198:205], v[96:99]
	v_mfma_f32_16x16x128_f8f6f4 v[166:169], v[150:157], v[206:213], v[84:87]
	v_mfma_f32_16x16x128_f8f6f4 v[170:173], v[158:165], v[206:213], v[80:83]
	v_mfma_f32_16x16x128_f8f6f4 v[194:197], v[150:157], v[214:221], v[68:71]
	v_mfma_f32_16x16x128_f8f6f4 v[198:201], v[158:165], v[214:221], v[64:67]
	s_setprio 0
	s_barrier
	s_mov_b32 m0, s66
	s_nop 3
	ds_read_b128 v[64:67], v149 offset:16384
	ds_read_b128 v[68:71], v149 offset:17408
	ds_read_b128 v[72:75], v149 offset:18432
	ds_read_b128 v[76:79], v149 offset:19456
	ds_read_b128 v[80:83], v149 offset:20480
	ds_read_b128 v[84:87], v149 offset:21504
	ds_read_b128 v[88:91], v149 offset:22528
	ds_read_b128 v[92:95], v149 offset:23552
	buffer_load_dwordx4 v144, s[48:51], s19 offen lds
	s_mov_b32 m0, s67
	s_add_i32 s21, s19, 0x40000
	buffer_load_dwordx4 v145, s[48:51], s19 offen lds
	s_mov_b32 m0, s68
	s_nop 0
	buffer_load_dwordx4 v144, s[48:51], s21 offen lds
	s_mov_b32 m0, s69
	s_nop 0
	buffer_load_dwordx4 v145, s[48:51], s21 offen lds
	s_mov_b32 m0, s63
	s_nop 0
	buffer_load_dwordx4 v146, s[44:47], s19 offen lds
	s_mov_b32 m0, s70
	s_nop 0
	buffer_load_dwordx4 v147, s[44:47], s19 offen lds
	s_waitcnt vmcnt(8)
	s_waitcnt lgkmcnt(0)
	s_barrier
	s_setprio 1
	s_waitcnt lgkmcnt(6)
	v_mfma_f32_16x16x128_f8f6f4 v[60:63], v[128:135], v[64:71], v[60:63]
	v_mfma_f32_16x16x128_f8f6f4 v[0:3], v[136:143], v[64:71], v[0:3]
	s_waitcnt lgkmcnt(4)
	v_mfma_f32_16x16x128_f8f6f4 v[202:205], v[128:135], v[72:79], v[48:51]
	v_mfma_f32_16x16x128_f8f6f4 v[206:209], v[136:143], v[72:79], v[44:47]
	s_waitcnt lgkmcnt(2)
	v_mfma_f32_16x16x128_f8f6f4 v[210:213], v[128:135], v[80:87], v[32:35]
	v_mfma_f32_16x16x128_f8f6f4 v[214:217], v[136:143], v[80:87], v[28:31]
	s_waitcnt lgkmcnt(0)
	v_mfma_f32_16x16x128_f8f6f4 v[218:221], v[128:135], v[88:95], v[16:19]
	v_mfma_f32_16x16x128_f8f6f4 v[222:225], v[136:143], v[88:95], v[12:15]
	s_setprio 0
	s_setprio 1
	v_mfma_f32_16x16x128_f8f6f4 v[56:59], v[150:157], v[64:71], v[56:59]
	v_mfma_f32_16x16x128_f8f6f4 v[52:55], v[158:165], v[64:71], v[52:55]
	v_mfma_f32_16x16x128_f8f6f4 v[226:229], v[150:157], v[72:79], v[40:43]
	v_mfma_f32_16x16x128_f8f6f4 v[232:235], v[158:165], v[72:79], v[36:39]
	v_mfma_f32_16x16x128_f8f6f4 v[236:239], v[150:157], v[80:87], v[24:27]
	v_mfma_f32_16x16x128_f8f6f4 v[240:243], v[158:165], v[80:87], v[20:23]
	v_mfma_f32_16x16x128_f8f6f4 v[244:247], v[150:157], v[88:95], v[8:11]
	v_mfma_f32_16x16x128_f8f6f4 v[248:251], v[158:165], v[88:95], v[4:7]
	s_setprio 0
	s_barrier
	v_add_u32_e32 v12, 0x18000, v148
	s_nop 3
	ds_read_b128 v[4:7], v12
	ds_read_b128 v[8:11], v12 offset:1024
	ds_read_b128 v[20:23], v12 offset:2048
	ds_read_b128 v[24:27], v12 offset:3072
	v_add_u32_e32 v12, 0x1c000, v148
	ds_read_b128 v[128:131], v12
	ds_read_b128 v[132:135], v12 offset:1024
	ds_read_b128 v[136:139], v12 offset:2048
	ds_read_b128 v[140:143], v12 offset:3072
	s_mov_b32 m0, s71
	ds_read_b128 v[12:15], v149 offset:32768
	ds_read_b128 v[16:19], v149 offset:33792
	ds_read_b128 v[28:31], v149 offset:34816
	ds_read_b128 v[32:35], v149 offset:35840
	ds_read_b128 v[36:39], v149 offset:36864
	ds_read_b128 v[40:43], v149 offset:37888
	ds_read_b128 v[44:47], v149 offset:38912
	ds_read_b128 v[48:51], v149 offset:39936
	buffer_load_dwordx4 v146, s[44:47], s21 offen lds
	s_mov_b32 m0, s72
	s_nop 0
	buffer_load_dwordx4 v147, s[44:47], s21 offen lds
	s_waitcnt vmcnt(8)
	s_waitcnt lgkmcnt(0)
	s_barrier
	s_setprio 1
	s_waitcnt lgkmcnt(6)
	v_mfma_f32_16x16x128_f8f6f4 v[124:127], v[4:11], v[12:19], v[124:127]
	v_mfma_f32_16x16x128_f8f6f4 v[120:123], v[20:27], v[12:19], v[120:123]
	s_waitcnt lgkmcnt(4)
	v_mfma_f32_16x16x128_f8f6f4 v[108:111], v[4:11], v[28:35], v[108:111]
	v_mfma_f32_16x16x128_f8f6f4 v[104:107], v[20:27], v[28:35], v[104:107]
	s_waitcnt lgkmcnt(2)
	v_mfma_f32_16x16x128_f8f6f4 v[92:95], v[4:11], v[36:43], v[178:181]
	v_mfma_f32_16x16x128_f8f6f4 v[88:91], v[20:27], v[36:43], v[182:185]
	s_waitcnt lgkmcnt(0)
	v_mfma_f32_16x16x128_f8f6f4 v[76:79], v[4:11], v[44:51], v[186:189]
	v_mfma_f32_16x16x128_f8f6f4 v[72:75], v[20:27], v[44:51], v[190:193]
	s_setprio 0
	s_setprio 1
	v_mfma_f32_16x16x128_f8f6f4 v[116:119], v[128:135], v[12:19], v[116:119]
	v_mfma_f32_16x16x128_f8f6f4 v[112:115], v[136:143], v[12:19], v[112:115]
	v_mfma_f32_16x16x128_f8f6f4 v[100:103], v[128:135], v[28:35], v[100:103]
	v_mfma_f32_16x16x128_f8f6f4 v[96:99], v[136:143], v[28:35], v[96:99]
	v_mfma_f32_16x16x128_f8f6f4 v[84:87], v[128:135], v[36:43], v[166:169]
	v_mfma_f32_16x16x128_f8f6f4 v[80:83], v[136:143], v[36:43], v[170:173]
	v_mfma_f32_16x16x128_f8f6f4 v[68:71], v[128:135], v[44:51], v[194:197]
	v_mfma_f32_16x16x128_f8f6f4 v[64:67], v[136:143], v[44:51], v[198:201]
	s_setprio 0
	s_barrier
	s_mov_b32 m0, s76
	s_or_b32 s21, s19, 0x80
	ds_read_b128 v[36:39], v149 offset:49152
	ds_read_b128 v[40:43], v149 offset:50176
	ds_read_b128 v[150:153], v149 offset:51200
	ds_read_b128 v[154:157], v149 offset:52224
	ds_read_b128 v[158:161], v149 offset:53248
	ds_read_b128 v[162:165], v149 offset:54272
	ds_read_b128 v[166:169], v149 offset:55296
	ds_read_b128 v[170:173], v149 offset:56320
	buffer_load_dwordx4 v144, s[48:51], s21 offen lds
	s_mov_b32 m0, s77
	s_add_i32 s19, s19, 0x40080
	buffer_load_dwordx4 v145, s[48:51], s21 offen lds
	s_mov_b32 m0, s80
	s_nop 0
	buffer_load_dwordx4 v144, s[48:51], s19 offen lds
	s_mov_b32 m0, s82
	s_nop 0
	buffer_load_dwordx4 v145, s[48:51], s19 offen lds
	s_mov_b32 m0, s78
	s_nop 0
	buffer_load_dwordx4 v146, s[44:47], s21 offen lds
	s_mov_b32 m0, s79
	s_nop 0
	buffer_load_dwordx4 v147, s[44:47], s21 offen lds
	s_waitcnt vmcnt(8)
	s_waitcnt lgkmcnt(0)
	s_barrier
	s_setprio 1
	s_waitcnt lgkmcnt(6)
	v_mfma_f32_16x16x128_f8f6f4 v[60:63], v[4:11], v[36:43], v[60:63]
	v_mfma_f32_16x16x128_f8f6f4 v[0:3], v[20:27], v[36:43], v[0:3]
	s_waitcnt lgkmcnt(4)
	v_mfma_f32_16x16x128_f8f6f4 v[48:51], v[4:11], v[150:157], v[202:205]
	v_mfma_f32_16x16x128_f8f6f4 v[44:47], v[20:27], v[150:157], v[206:209]
	s_waitcnt lgkmcnt(2)
	v_mfma_f32_16x16x128_f8f6f4 v[32:35], v[4:11], v[158:165], v[210:213]
	v_mfma_f32_16x16x128_f8f6f4 v[28:31], v[20:27], v[158:165], v[214:217]
	s_waitcnt lgkmcnt(0)
	v_mfma_f32_16x16x128_f8f6f4 v[16:19], v[4:11], v[166:173], v[218:221]
	v_mfma_f32_16x16x128_f8f6f4 v[12:15], v[20:27], v[166:173], v[222:225]
	s_setprio 0
	s_setprio 1
	v_mfma_f32_16x16x128_f8f6f4 v[56:59], v[128:135], v[36:43], v[56:59]
	v_mfma_f32_16x16x128_f8f6f4 v[52:55], v[136:143], v[36:43], v[52:55]
	v_mfma_f32_16x16x128_f8f6f4 v[40:43], v[128:135], v[150:157], v[226:229]
	v_mfma_f32_16x16x128_f8f6f4 v[36:39], v[136:143], v[150:157], v[232:235]
	v_mfma_f32_16x16x128_f8f6f4 v[24:27], v[128:135], v[158:165], v[236:239]
	v_mfma_f32_16x16x128_f8f6f4 v[20:23], v[136:143], v[158:165], v[240:243]
	v_mfma_f32_16x16x128_f8f6f4 v[8:11], v[128:135], v[166:173], v[244:247]
	v_mfma_f32_16x16x128_f8f6f4 v[4:7], v[136:143], v[166:173], v[248:251]
	s_setprio 0
	s_barrier
	s_add_i32 s12, s12, 2
	s_addk_i32 s13, 0x100
	s_cmp_gt_u32 s12, 13
	s_cbranch_scc0 .LBB0_1187
	s_and_b64 vcc, exec, s[8:9]
	s_cbranch_vccz .LBB0_1190
	s_barrier

.LBB0_1507:
	v_add_u32_e32 v116, 0x10000, v176
	v_add_u32_e32 v120, 0x14000, v176
	ds_read_b128 v[104:107], v116
	ds_read_b128 v[108:111], v116 offset:1024
	ds_read_b128 v[112:115], v116 offset:2048
	ds_read_b128 v[116:119], v116 offset:3072
	ds_read_b128 v[148:151], v120
	ds_read_b128 v[152:155], v120 offset:1024
	ds_read_b128 v[156:159], v120 offset:2048
	ds_read_b128 v[160:163], v120 offset:3072
	s_add_i32 s21, s13, 0xfffc0080
	s_cmp_eq_u32 s12, 12
	s_cselect_b32 s45, s29, s41
	s_cselect_b32 s44, s28, s40
	s_cselect_b32 s47, s31, s43
	s_cselect_b32 s46, s30, s42
	s_cselect_b32 s21, 0, s21
	s_cselect_b32 s49, s35, s53
	s_cselect_b32 s48, s34, s52
	s_cselect_b32 s51, s39, s5
	s_cselect_b32 s50, s38, s4
	s_mov_b32 m0, s90
	ds_read_b128 v[164:167], v198
	ds_read_b128 v[168:171], v198 offset:1024
	ds_read_b128 v[200:203], v198 offset:2048
	ds_read_b128 v[204:207], v198 offset:3072
	ds_read_b128 v[208:211], v198 offset:4096
	ds_read_b128 v[212:215], v198 offset:5120
	ds_read_b128 v[216:219], v198 offset:6144
	ds_read_b128 v[220:223], v198 offset:7168
	buffer_load_dwordx4 v229, s[40:43], s13 offen lds
	s_mov_b32 m0, s92
	s_nop 0
	buffer_load_dwordx4 v252, s[40:43], s13 offen lds
	s_waitcnt vmcnt(8)
	s_waitcnt lgkmcnt(0)
	s_barrier
	s_setprio 1
	s_waitcnt lgkmcnt(6)
	v_mfma_f32_16x16x128_f8f6f4 v[140:143], v[112:119], v[164:171], v[140:143]
	s_waitcnt lgkmcnt(4)
	v_mfma_f32_16x16x128_f8f6f4 v[128:131], v[104:111], v[200:207], v[128:131]
	v_mfma_f32_16x16x128_f8f6f4 v[124:127], v[112:119], v[200:207], v[124:127]
	v_mfma_f32_16x16x128_f8f6f4 v[120:123], v[104:111], v[164:171], v[144:147]
	s_waitcnt lgkmcnt(2)
	v_mfma_f32_16x16x128_f8f6f4 v[178:181], v[104:111], v[208:215], v[92:95]
	v_mfma_f32_16x16x128_f8f6f4 v[182:185], v[112:119], v[208:215], v[88:91]
	s_waitcnt lgkmcnt(0)
	v_mfma_f32_16x16x128_f8f6f4 v[186:189], v[104:111], v[216:223], v[76:79]
	v_mfma_f32_16x16x128_f8f6f4 v[190:193], v[112:119], v[216:223], v[72:75]
	s_setprio 0
	s_setprio 1
	v_mfma_f32_16x16x128_f8f6f4 v[136:139], v[148:155], v[164:171], v[136:139]
	v_mfma_f32_16x16x128_f8f6f4 v[132:135], v[156:163], v[164:171], v[132:135]
	v_mfma_f32_16x16x128_f8f6f4 v[100:103], v[148:155], v[200:207], v[100:103]
	v_mfma_f32_16x16x128_f8f6f4 v[96:99], v[156:163], v[200:207], v[96:99]
	v_mfma_f32_16x16x128_f8f6f4 v[164:167], v[148:155], v[208:215], v[84:87]
	v_mfma_f32_16x16x128_f8f6f4 v[168:171], v[156:163], v[208:215], v[80:83]
	v_mfma_f32_16x16x128_f8f6f4 v[194:197], v[148:155], v[216:223], v[68:71]
	v_mfma_f32_16x16x128_f8f6f4 v[200:203], v[156:163], v[216:223], v[64:67]
	s_setprio 0
	s_barrier
	s_mov_b32 m0, s63
	s_nop 3
	ds_read_b128 v[64:67], v198 offset:16384
	ds_read_b128 v[68:71], v198 offset:17408
	ds_read_b128 v[72:75], v198 offset:18432
	ds_read_b128 v[76:79], v198 offset:19456
	ds_read_b128 v[80:83], v198 offset:20480
	ds_read_b128 v[84:87], v198 offset:21504
	ds_read_b128 v[88:91], v198 offset:22528
	ds_read_b128 v[92:95], v198 offset:23552
	buffer_load_dwordx4 v199, s[48:51], s21 offen lds
	s_mov_b32 m0, s69
	s_add_i32 s23, s21, 0x40000
	buffer_load_dwordx4 v228, s[48:51], s21 offen lds
	s_mov_b32 m0, s70
	s_nop 0
	buffer_load_dwordx4 v199, s[48:51], s23 offen lds
	s_mov_b32 m0, s71
	s_nop 0
	buffer_load_dwordx4 v228, s[48:51], s23 offen lds
	s_mov_b32 m0, s62
	s_nop 0
	buffer_load_dwordx4 v229, s[44:47], s21 offen lds
	s_mov_b32 m0, s72
	s_nop 0
	buffer_load_dwordx4 v252, s[44:47], s21 offen lds
	s_waitcnt vmcnt(8)
	s_waitcnt lgkmcnt(0)
	s_barrier
	s_setprio 1
	s_waitcnt lgkmcnt(6)
	v_mfma_f32_16x16x128_f8f6f4 v[60:63], v[104:111], v[64:71], v[60:63]
	s_waitcnt lgkmcnt(0)
	v_mfma_f32_16x16x128_f8f6f4 v[16:19], v[104:111], v[88:95], v[16:19]
	v_mfma_f32_16x16x128_f8f6f4 v[204:207], v[112:119], v[64:71], v[8:11]
	v_mfma_f32_16x16x128_f8f6f4 v[208:211], v[104:111], v[72:79], v[48:51]
	v_mfma_f32_16x16x128_f8f6f4 v[212:215], v[112:119], v[72:79], v[44:47]
	v_mfma_f32_16x16x128_f8f6f4 v[216:219], v[104:111], v[80:87], v[32:35]
	v_mfma_f32_16x16x128_f8f6f4 v[220:223], v[112:119], v[80:87], v[28:31]
	v_mfma_f32_16x16x128_f8f6f4 v[224:227], v[112:119], v[88:95], v[12:15]
	s_setprio 0
	s_setprio 1
	v_mfma_f32_16x16x128_f8f6f4 v[56:59], v[148:155], v[64:71], v[56:59]
	v_mfma_f32_16x16x128_f8f6f4 v[52:55], v[156:163], v[64:71], v[52:55]
	v_mfma_f32_16x16x128_f8f6f4 v[232:235], v[148:155], v[72:79], v[40:43]
	v_mfma_f32_16x16x128_f8f6f4 v[236:239], v[156:163], v[72:79], v[36:39]
	v_mfma_f32_16x16x128_f8f6f4 v[240:243], v[148:155], v[80:87], v[24:27]
	v_mfma_f32_16x16x128_f8f6f4 v[244:247], v[156:163], v[80:87], v[20:23]
	v_mfma_f32_16x16x128_f8f6f4 v[248:251], v[148:155], v[88:95], v[4:7]
	v_mfma_f32_16x16x128_f8f6f4 v[172:175], v[156:163], v[88:95], v[0:3]
	s_setprio 0
	s_barrier
	v_add_u32_e32 v8, 0x18000, v176
	s_nop 3
	ds_read_b128 v[0:3], v8
	ds_read_b128 v[4:7], v8 offset:1024
	ds_read_b128 v[20:23], v8 offset:2048
	ds_read_b128 v[24:27], v8 offset:3072
	v_add_u32_e32 v8, 0x1c000, v176
	ds_read_b128 v[104:107], v8
	ds_read_b128 v[108:111], v8 offset:1024
	ds_read_b128 v[112:115], v8 offset:2048
	ds_read_b128 v[116:119], v8 offset:3072
	s_mov_b32 m0, s73
	ds_read_b128 v[8:11], v198 offset:32768
	ds_read_b128 v[12:15], v198 offset:33792
	ds_read_b128 v[28:31], v198 offset:34816
	ds_read_b128 v[32:35], v198 offset:35840
	ds_read_b128 v[36:39], v198 offset:36864
	ds_read_b128 v[40:43], v198 offset:37888
	ds_read_b128 v[44:47], v198 offset:38912
	ds_read_b128 v[48:51], v198 offset:39936
	buffer_load_dwordx4 v229, s[44:47], s23 offen lds
	s_mov_b32 m0, s74
	s_nop 0
	buffer_load_dwordx4 v252, s[44:47], s23 offen lds
	s_waitcnt vmcnt(8)
	s_waitcnt lgkmcnt(0)
	s_barrier
	s_setprio 1
	s_waitcnt lgkmcnt(6)
	v_mfma_f32_16x16x128_f8f6f4 v[144:147], v[0:7], v[8:15], v[120:123]
	v_mfma_f32_16x16x128_f8f6f4 v[140:143], v[20:27], v[8:15], v[140:143]
	s_waitcnt lgkmcnt(4)
	v_mfma_f32_16x16x128_f8f6f4 v[128:131], v[0:7], v[28:35], v[128:131]
	v_mfma_f32_16x16x128_f8f6f4 v[124:127], v[20:27], v[28:35], v[124:127]
	s_waitcnt lgkmcnt(2)
	v_mfma_f32_16x16x128_f8f6f4 v[92:95], v[0:7], v[36:43], v[178:181]
	v_mfma_f32_16x16x128_f8f6f4 v[88:91], v[20:27], v[36:43], v[182:185]
	s_waitcnt lgkmcnt(0)
	v_mfma_f32_16x16x128_f8f6f4 v[76:79], v[0:7], v[44:51], v[186:189]
	v_mfma_f32_16x16x128_f8f6f4 v[72:75], v[20:27], v[44:51], v[190:193]
	s_setprio 0
	s_setprio 1
	v_mfma_f32_16x16x128_f8f6f4 v[136:139], v[104:111], v[8:15], v[136:139]
	v_mfma_f32_16x16x128_f8f6f4 v[132:135], v[112:119], v[8:15], v[132:135]
	v_mfma_f32_16x16x128_f8f6f4 v[100:103], v[104:111], v[28:35], v[100:103]
	v_mfma_f32_16x16x128_f8f6f4 v[96:99], v[112:119], v[28:35], v[96:99]
	v_mfma_f32_16x16x128_f8f6f4 v[84:87], v[104:111], v[36:43], v[164:167]
	v_mfma_f32_16x16x128_f8f6f4 v[80:83], v[112:119], v[36:43], v[168:171]
	v_mfma_f32_16x16x128_f8f6f4 v[68:71], v[104:111], v[44:51], v[194:197]
	v_mfma_f32_16x16x128_f8f6f4 v[64:67], v[112:119], v[44:51], v[200:203]
	s_setprio 0
	s_barrier
	s_mov_b32 m0, s75
	s_or_b32 s23, s21, 0x80
	ds_read_b128 v[36:39], v198 offset:49152
	ds_read_b128 v[40:43], v198 offset:50176
	ds_read_b128 v[148:151], v198 offset:51200
	ds_read_b128 v[152:155], v198 offset:52224
	ds_read_b128 v[156:159], v198 offset:53248
	ds_read_b128 v[160:163], v198 offset:54272
	ds_read_b128 v[164:167], v198 offset:55296
	ds_read_b128 v[168:171], v198 offset:56320
	buffer_load_dwordx4 v199, s[48:51], s23 offen lds
	s_mov_b32 m0, s76
	s_add_i32 s21, s21, 0x40080
	buffer_load_dwordx4 v228, s[48:51], s23 offen lds
	s_mov_b32 m0, s82
	s_nop 0
	buffer_load_dwordx4 v199, s[48:51], s21 offen lds
	s_mov_b32 m0, s83
	s_nop 0
	buffer_load_dwordx4 v228, s[48:51], s21 offen lds
	s_mov_b32 m0, s77
	s_nop 0
	buffer_load_dwordx4 v229, s[44:47], s23 offen lds
	s_mov_b32 m0, s80
	s_nop 0
	buffer_load_dwordx4 v252, s[44:47], s23 offen lds
	s_waitcnt vmcnt(8)
	s_waitcnt lgkmcnt(0)
	s_barrier
	s_setprio 1
	s_waitcnt lgkmcnt(6)
	v_mfma_f32_16x16x128_f8f6f4 v[60:63], v[0:7], v[36:43], v[60:63]
	v_mfma_f32_16x16x128_f8f6f4 v[8:11], v[20:27], v[36:43], v[204:207]
	s_waitcnt lgkmcnt(4)
	v_mfma_f32_16x16x128_f8f6f4 v[48:51], v[0:7], v[148:155], v[208:211]
	v_mfma_f32_16x16x128_f8f6f4 v[44:47], v[20:27], v[148:155], v[212:215]
	s_waitcnt lgkmcnt(2)
	v_mfma_f32_16x16x128_f8f6f4 v[32:35], v[0:7], v[156:163], v[216:219]
	v_mfma_f32_16x16x128_f8f6f4 v[28:31], v[20:27], v[156:163], v[220:223]
	s_waitcnt lgkmcnt(0)
	v_mfma_f32_16x16x128_f8f6f4 v[16:19], v[0:7], v[164:171], v[16:19]
	v_mfma_f32_16x16x128_f8f6f4 v[12:15], v[20:27], v[164:171], v[224:227]
	s_setprio 0
	s_setprio 1
	v_mfma_f32_16x16x128_f8f6f4 v[56:59], v[104:111], v[36:43], v[56:59]
	v_mfma_f32_16x16x128_f8f6f4 v[52:55], v[112:119], v[36:43], v[52:55]
	v_mfma_f32_16x16x128_f8f6f4 v[40:43], v[104:111], v[148:155], v[232:235]
	v_mfma_f32_16x16x128_f8f6f4 v[36:39], v[112:119], v[148:155], v[236:239]
	v_mfma_f32_16x16x128_f8f6f4 v[24:27], v[104:111], v[156:163], v[240:243]
	v_mfma_f32_16x16x128_f8f6f4 v[20:23], v[112:119], v[156:163], v[244:247]
	v_mfma_f32_16x16x128_f8f6f4 v[4:7], v[104:111], v[164:171], v[248:251]
	v_mfma_f32_16x16x128_f8f6f4 v[0:3], v[112:119], v[164:171], v[172:175]
	s_setprio 0
	s_barrier
	s_add_i32 s12, s12, 2
	s_addk_i32 s13, 0x100
	s_cmp_gt_u32 s12, 13
	s_cbranch_scc0 .LBB0_1507
	s_and_b64 vcc, exec, s[18:19]
	s_cbranch_vccz .LBB0_1510
	s_barrier

.LBB0_1723:
	s_nop 0
	v_add_u32_e32 v64, 0x10000, v138
	ds_read_b128 v[140:143], v64
	ds_read_b128 v[144:147], v64 offset:1024
	ds_read_b128 v[148:151], v64 offset:2048
	ds_read_b128 v[152:155], v64 offset:3072
	v_add_u32_e32 v64, 0x14000, v138
	ds_read_b128 v[156:159], v64
	ds_read_b128 v[160:163], v64 offset:1024
	ds_read_b128 v[164:167], v64 offset:2048
	ds_read_b128 v[168:171], v64 offset:3072
	s_cmp_eq_u32 s12, 12
	s_cselect_b64 s[4:5], -1, 0
	s_and_b64 s[48:49], s[4:5], exec
	s_cselect_b32 s31, 0, s13
	s_cselect_b32 s49, s35, s45
	s_cselect_b32 s48, s34, s44
	s_cselect_b32 s51, s43, s47
	s_cselect_b32 s50, s42, s46
	s_cselect_b32 s56, s62, s40
	s_cselect_b32 s57, s63, s41
	s_cselect_b32 s58, s64, s66
	s_cselect_b32 s59, s65, s67
	s_or_b32 vcc_lo, s31, 0x80
	s_add_i32 vcc_hi, s13, 0xffffff80
	ds_read_b128 v[198:201], v139
	ds_read_b128 v[202:205], v139 offset:1024
	ds_read_b128 v[206:209], v139 offset:2048
	ds_read_b128 v[210:213], v139 offset:3072
	ds_read_b128 v[214:217], v139 offset:4096
	ds_read_b128 v[218:221], v139 offset:5120
	ds_read_b128 v[222:225], v139 offset:6144
	ds_read_b128 v[226:229], v139 offset:7168
	v_mbcnt_lo_u32_b32 v64, -1, 0
	v_mbcnt_hi_u32_b32 v64, -1, v64
	s_mov_b32 m0, s93
	v_lshl_add_u32 v64, v64, 4, s71
	ds_read_b64 v[64:65], v64 offset:8
	s_waitcnt lgkmcnt(0)
	buffer_load_dwordx4 v64, s[44:47], vcc_hi offen lds
	s_mov_b32 m0, s96
	s_nop 0
	buffer_load_dwordx4 v65, s[44:47], vcc_hi offen lds
	s_waitcnt vmcnt(8)
	s_waitcnt lgkmcnt(0)
	s_barrier
	s_setprio 1
	v_mfma_f32_16x16x128_f8f6f4 v[128:131], v[148:155], v[198:205], v[128:131]
	v_mfma_f32_16x16x128_f8f6f4 v[108:111], v[140:147], v[206:213], v[108:111]
	v_mfma_f32_16x16x128_f8f6f4 v[104:107], v[148:155], v[206:213], v[104:107]
	v_mfma_f32_16x16x128_f8f6f4 v[112:115], v[140:147], v[198:205], v[124:127]
	v_mfma_f32_16x16x128_f8f6f4 v[132:135], v[140:147], v[214:221], v[92:95]
	v_mfma_f32_16x16x128_f8f6f4 v[172:175], v[148:155], v[214:221], v[88:91]
	v_mfma_f32_16x16x128_f8f6f4 v[178:181], v[140:147], v[222:229], v[76:79]
	v_mfma_f32_16x16x128_f8f6f4 v[182:185], v[148:155], v[222:229], v[72:75]
	s_setprio 0
	s_setprio 1
	v_mfma_f32_16x16x128_f8f6f4 v[120:123], v[156:163], v[198:205], v[120:123]
	v_mfma_f32_16x16x128_f8f6f4 v[116:119], v[164:171], v[198:205], v[116:119]
	v_mfma_f32_16x16x128_f8f6f4 v[100:103], v[156:163], v[206:213], v[100:103]
	v_mfma_f32_16x16x128_f8f6f4 v[96:99], v[164:171], v[206:213], v[96:99]
	v_mfma_f32_16x16x128_f8f6f4 v[186:189], v[156:163], v[214:221], v[84:87]
	v_mfma_f32_16x16x128_f8f6f4 v[190:193], v[164:171], v[214:221], v[80:83]
	v_mfma_f32_16x16x128_f8f6f4 v[194:197], v[156:163], v[222:229], v[68:71]
	v_mfma_f32_16x16x128_f8f6f4 v[198:201], v[164:171], v[222:229], v[24:27]
	s_setprio 0
	s_barrier
	s_mov_b32 m0, s74
	s_add_i32 vcc_hi, s31, 0x40000
	s_and_b64 s[4:5], s[38:39], s[4:5]
	ds_read_b128 v[64:67], v139 offset:16384
	ds_read_b128 v[68:71], v139 offset:17408
	ds_read_b128 v[72:75], v139 offset:18432
	ds_read_b128 v[76:79], v139 offset:19456
	ds_read_b128 v[80:83], v139 offset:20480
	ds_read_b128 v[84:87], v139 offset:21504
	ds_read_b128 v[88:91], v139 offset:22528
	ds_read_b128 v[92:95], v139 offset:23552
	buffer_load_dwordx4 v136, s[56:59], s31 offen lds
	s_mov_b32 m0, s75
	s_and_b64 s[4:5], s[4:5], exec
	buffer_load_dwordx4 v137, s[56:59], s31 offen lds
	s_mov_b32 m0, s76
	s_mov_b32 s4, 0x24000
	buffer_load_dwordx4 v136, s[56:59], vcc_hi offen lds
	s_mov_b32 m0, s77
	s_cselect_b32 s4, s4, 0x20500
	buffer_load_dwordx4 v137, s[56:59], vcc_hi offen lds
	v_mbcnt_lo_u32_b32 v24, -1, 0
	v_mbcnt_hi_u32_b32 v24, -1, v24
	s_add_i32 s4, s70, s4
	v_lshl_add_u32 v24, v24, 4, s4
	ds_read_b64 v[24:25], v24
	s_mov_b32 m0, s70
	s_waitcnt lgkmcnt(0)
	buffer_load_dwordx4 v24, s[48:51], s31 offen lds
	s_mov_b32 m0, s78
	s_nop 0
	buffer_load_dwordx4 v25, s[48:51], s31 offen lds
	s_waitcnt vmcnt(8)
	s_waitcnt lgkmcnt(0)
	s_barrier
	s_setprio 1
	v_mfma_f32_16x16x128_f8f6f4 v[60:63], v[140:147], v[64:71], v[60:63]
	v_mfma_f32_16x16x128_f8f6f4 v[0:3], v[148:155], v[64:71], v[0:3]
	v_mfma_f32_16x16x128_f8f6f4 v[12:15], v[140:147], v[88:95], v[12:15]
	v_mfma_f32_16x16x128_f8f6f4 v[206:209], v[140:147], v[72:79], v[44:47]
	v_mfma_f32_16x16x128_f8f6f4 v[210:213], v[148:155], v[72:79], v[48:51]
	v_mfma_f32_16x16x128_f8f6f4 v[214:217], v[140:147], v[80:87], v[28:31]
	v_mfma_f32_16x16x128_f8f6f4 v[218:221], v[148:155], v[80:87], v[32:35]
	v_mfma_f32_16x16x128_f8f6f4 v[222:225], v[148:155], v[88:95], v[16:19]
	s_setprio 0
	s_setprio 1
	v_mfma_f32_16x16x128_f8f6f4 v[56:59], v[164:171], v[64:71], v[56:59]
	v_mfma_f32_16x16x128_f8f6f4 v[244:247], v[164:171], v[80:87], v[244:247]
	v_mfma_f32_16x16x128_f8f6f4 v[226:229], v[156:163], v[64:71], v[52:55]
	v_mfma_f32_16x16x128_f8f6f4 v[232:235], v[156:163], v[72:79], v[36:39]
	v_mfma_f32_16x16x128_f8f6f4 v[236:239], v[164:171], v[72:79], v[40:43]
	v_mfma_f32_16x16x128_f8f6f4 v[240:243], v[156:163], v[80:87], v[20:23]
	v_mfma_f32_16x16x128_f8f6f4 v[248:251], v[156:163], v[88:95], v[4:7]
	v_mfma_f32_16x16x128_f8f6f4 v[64:67], v[164:171], v[88:95], v[8:11]
	s_setprio 0
	s_barrier
	s_nop 2
	v_add_u32_e32 v20, 0x18000, v138
	v_add_u32_e32 v24, 0x1c000, v138
	ds_read_b128 v[4:7], v20
	ds_read_b128 v[8:11], v20 offset:1024
	ds_read_b128 v[16:19], v20 offset:2048
	ds_read_b128 v[20:23], v20 offset:3072
	ds_read_b128 v[140:143], v24
	ds_read_b128 v[144:147], v24 offset:1024
	ds_read_b128 v[148:151], v24 offset:2048
	ds_read_b128 v[152:155], v24 offset:3072
	ds_read_b128 v[24:27], v139 offset:32768
	ds_read_b128 v[28:31], v139 offset:33792
	ds_read_b128 v[32:35], v139 offset:34816
	ds_read_b128 v[36:39], v139 offset:35840
	ds_read_b128 v[40:43], v139 offset:36864
	ds_read_b128 v[44:47], v139 offset:37888
	ds_read_b128 v[48:51], v139 offset:38912
	ds_read_b128 v[52:55], v139 offset:39936
	v_mbcnt_lo_u32_b32 v68, -1, 0
	v_mbcnt_hi_u32_b32 v68, -1, v68
	s_mov_b32 m0, s79
	v_lshl_add_u32 v68, v68, 4, s4
	ds_read_b64 v[68:69], v68 offset:8
	s_waitcnt lgkmcnt(0)
	buffer_load_dwordx4 v68, s[48:51], s31 offen lds
	s_mov_b32 m0, s80
	s_nop 0
	buffer_load_dwordx4 v69, s[48:51], s31 offen lds
	s_waitcnt vmcnt(8)
	s_waitcnt lgkmcnt(0)
	s_barrier
	s_setprio 1
	v_mfma_f32_16x16x128_f8f6f4 v[124:127], v[4:11], v[24:31], v[112:115]
	v_mfma_f32_16x16x128_f8f6f4 v[128:131], v[16:23], v[24:31], v[128:131]
	v_mfma_f32_16x16x128_f8f6f4 v[108:111], v[4:11], v[32:39], v[108:111]
	v_mfma_f32_16x16x128_f8f6f4 v[104:107], v[16:23], v[32:39], v[104:107]
	v_mfma_f32_16x16x128_f8f6f4 v[92:95], v[4:11], v[40:47], v[132:135]
	v_mfma_f32_16x16x128_f8f6f4 v[88:91], v[16:23], v[40:47], v[172:175]
	v_mfma_f32_16x16x128_f8f6f4 v[76:79], v[4:11], v[48:55], v[178:181]
	v_mfma_f32_16x16x128_f8f6f4 v[72:75], v[16:23], v[48:55], v[182:185]
	s_setprio 0
	s_setprio 1
	v_mfma_f32_16x16x128_f8f6f4 v[120:123], v[140:147], v[24:31], v[120:123]
	v_mfma_f32_16x16x128_f8f6f4 v[116:119], v[148:155], v[24:31], v[116:119]
	v_mfma_f32_16x16x128_f8f6f4 v[100:103], v[140:147], v[32:39], v[100:103]
	v_mfma_f32_16x16x128_f8f6f4 v[96:99], v[148:155], v[32:39], v[96:99]
	v_mfma_f32_16x16x128_f8f6f4 v[84:87], v[140:147], v[40:47], v[186:189]
	v_mfma_f32_16x16x128_f8f6f4 v[80:83], v[148:155], v[40:47], v[190:193]
	v_mfma_f32_16x16x128_f8f6f4 v[68:71], v[140:147], v[48:55], v[194:197]
	v_mfma_f32_16x16x128_f8f6f4 v[24:27], v[148:155], v[48:55], v[198:201]
	s_setprio 0
	s_barrier
	s_mov_b32 m0, s83
	ds_read_b128 v[36:39], v139 offset:49152
	ds_read_b128 v[40:43], v139 offset:50176
	ds_read_b128 v[156:159], v139 offset:51200
	ds_read_b128 v[160:163], v139 offset:52224
	ds_read_b128 v[164:167], v139 offset:53248
	ds_read_b128 v[168:171], v139 offset:54272
	ds_read_b128 v[198:201], v139 offset:55296
	ds_read_b128 v[202:205], v139 offset:56320
	buffer_load_dwordx4 v136, s[56:59], vcc_lo offen lds
	s_mov_b32 m0, s88
	s_add_i32 s31, s31, 0x40080
	buffer_load_dwordx4 v137, s[56:59], vcc_lo offen lds
	s_mov_b32 m0, s91
	s_nop 0
	buffer_load_dwordx4 v136, s[56:59], s31 offen lds
	s_mov_b32 m0, s92
	s_nop 0
	buffer_load_dwordx4 v137, s[56:59], s31 offen lds
	v_mbcnt_lo_u32_b32 v28, -1, 0
	v_mbcnt_hi_u32_b32 v28, -1, v28
	s_mov_b32 m0, s89
	v_lshl_add_u32 v28, v28, 4, s4
	ds_read_b64 v[28:29], v28
	s_waitcnt lgkmcnt(0)
	buffer_load_dwordx4 v28, s[48:51], vcc_lo offen lds
	s_mov_b32 m0, s90
	s_nop 0
	buffer_load_dwordx4 v29, s[48:51], vcc_lo offen lds
	s_waitcnt vmcnt(8)
	s_waitcnt lgkmcnt(0)
	s_barrier
	s_setprio 1
	v_mfma_f32_16x16x128_f8f6f4 v[60:63], v[4:11], v[36:43], v[60:63]
	v_mfma_f32_16x16x128_f8f6f4 v[0:3], v[16:23], v[36:43], v[0:3]
	v_mfma_f32_16x16x128_f8f6f4 v[44:47], v[4:11], v[156:163], v[206:209]
	v_mfma_f32_16x16x128_f8f6f4 v[48:51], v[16:23], v[156:163], v[210:213]
	v_mfma_f32_16x16x128_f8f6f4 v[28:31], v[4:11], v[164:171], v[214:217]
	v_mfma_f32_16x16x128_f8f6f4 v[32:35], v[16:23], v[164:171], v[218:221]
	v_mfma_f32_16x16x128_f8f6f4 v[12:15], v[4:11], v[198:205], v[12:15]
	v_mfma_f32_16x16x128_f8f6f4 v[16:19], v[16:23], v[198:205], v[222:225]
	s_setprio 0
	s_setprio 1
	v_mfma_f32_16x16x128_f8f6f4 v[52:55], v[140:147], v[36:43], v[226:229]
	v_mfma_f32_16x16x128_f8f6f4 v[56:59], v[148:155], v[36:43], v[56:59]
	v_mfma_f32_16x16x128_f8f6f4 v[36:39], v[140:147], v[156:163], v[232:235]
	v_mfma_f32_16x16x128_f8f6f4 v[40:43], v[148:155], v[156:163], v[236:239]
	v_mfma_f32_16x16x128_f8f6f4 v[20:23], v[140:147], v[164:171], v[240:243]
	v_mfma_f32_16x16x128_f8f6f4 v[244:247], v[148:155], v[164:171], v[244:247]
	v_mfma_f32_16x16x128_f8f6f4 v[4:7], v[140:147], v[198:205], v[248:251]
	v_mfma_f32_16x16x128_f8f6f4 v[8:11], v[148:155], v[198:205], v[64:67]
	s_setprio 0
	s_barrier
	s_add_i32 s12, s12, 2
	s_addk_i32 s13, 0x100
	s_cmp_gt_u32 s12, 13
	s_cbranch_scc0 .LBB0_1723
	s_mov_b64 s[4:5], 0
	s_and_b64 vcc, exec, s[38:39]
	s_cbranch_vccz .LBB0_1731
	v_readlane_b32 s4, v255, 9
	v_mov_b32_e32 v222, v176
	s_nop 0
	v_mov_b32_e32 v64, s4
	ds_read_b32 v64, v64
	s_add_i32 s4, s3, 2
	s_mul_i32 s3, s4, s72
	s_mul_hi_u32 s5, s4, s33
	s_add_i32 s5, s5, s3
	s_waitcnt lgkmcnt(0)
	v_readfirstlane_b32 s3, v64
	s_mul_i32 s4, s4, s33
	s_mul_i32 s31, s3, 44
	s_add_u32 s12, s4, s61
	s_addc_u32 s13, s5, s73
	s_ashr_i32 s38, s31, 31
	v_mov_b32_e32 v64, s31
	v_mov_b32_e32 v65, s38
	v_cmp_ge_i64_e32 vcc, s[12:13], v[64:65]
	s_mov_b64 s[4:5], 0
	s_cbranch_vccnz .LBB0_1732
	s_lshr_b32 s4, s38, 29
	s_add_i32 s4, s31, s4
	s_ashr_i32 s38, s4, 3
	s_and_b32 s4, s4, -8
	s_sub_i32 s39, s31, s4
	s_ashr_i32 s4, s12, 31
	s_lshr_b32 s4, s4, 29
	s_add_i32 s13, s12, s4
	s_and_b32 s4, s13, -8
	s_sub_i32 s12, s12, s4
	s_add_i32 s29, s38, 1
	s_cmp_ge_i32 s12, s39
	s_mov_b64 s[4:5], -1
	s_cbranch_scc0 .LBB0_1728
	s_sub_i32 s5, s12, s39
	s_mul_i32 s4, s29, s39
	s_mul_i32 s5, s5, s38
	s_add_i32 s31, s5, s4
	s_mov_b64 s[4:5], 0

.LBB0_1825:
	v_add_u32_e32 v128, 0x10000, v134
	ds_read_b128 v[136:139], v128
	ds_read_b128 v[140:143], v128 offset:1024
	ds_read_b128 v[144:147], v128 offset:2048
	ds_read_b128 v[148:151], v128 offset:3072
	v_add_u32_e32 v128, 0x14000, v134
	ds_read_b128 v[152:155], v128
	ds_read_b128 v[156:159], v128 offset:1024
	ds_read_b128 v[160:163], v128 offset:2048
	ds_read_b128 v[164:167], v128 offset:3072
	s_add_i32 s31, s13, 0xfff50080
	s_cmp_eq_u32 s12, 40
	s_cselect_b32 s45, s19, s41
	s_cselect_b32 s44, s18, s40
	s_cselect_b32 s47, s21, s43
	s_cselect_b32 s46, s20, s42
	s_cselect_b32 s31, 0, s31
	s_cselect_b32 s49, s23, s53
	s_cselect_b32 s48, s22, s52
	s_cselect_b32 s51, s29, s5
	s_cselect_b32 s50, s28, s4
	s_mov_b32 m0, s77
	ds_read_b128 v[168:171], v135
	ds_read_b128 v[172:175], v135 offset:1024
	ds_read_b128 v[198:201], v135 offset:2048
	ds_read_b128 v[202:205], v135 offset:3072
	ds_read_b128 v[206:209], v135 offset:4096
	ds_read_b128 v[210:213], v135 offset:5120
	ds_read_b128 v[214:217], v135 offset:6144
	ds_read_b128 v[218:221], v135 offset:7168
	buffer_load_dwordx4 v132, s[40:43], s13 offen lds
	s_mov_b32 m0, s79
	s_nop 0
	buffer_load_dwordx4 v133, s[40:43], s13 offen lds
	s_waitcnt vmcnt(8)
	s_waitcnt lgkmcnt(0)
	s_barrier
	s_setprio 1
	s_waitcnt lgkmcnt(6)
	v_mfma_f32_16x16x128_f8f6f4 v[124:127], v[136:143], v[168:175], v[124:127]
	v_mfma_f32_16x16x128_f8f6f4 v[120:123], v[144:151], v[168:175], v[120:123]
	s_waitcnt lgkmcnt(4)
	v_mfma_f32_16x16x128_f8f6f4 v[108:111], v[136:143], v[198:205], v[108:111]
	v_mfma_f32_16x16x128_f8f6f4 v[104:107], v[144:151], v[198:205], v[104:107]
	s_waitcnt lgkmcnt(2)
	v_mfma_f32_16x16x128_f8f6f4 v[178:181], v[136:143], v[206:213], v[92:95]
	v_mfma_f32_16x16x128_f8f6f4 v[182:185], v[144:151], v[206:213], v[88:91]
	s_waitcnt lgkmcnt(0)
	v_mfma_f32_16x16x128_f8f6f4 v[186:189], v[136:143], v[214:221], v[76:79]
	v_mfma_f32_16x16x128_f8f6f4 v[190:193], v[144:151], v[214:221], v[72:75]
	s_setprio 0
	s_setprio 1
	v_mfma_f32_16x16x128_f8f6f4 v[116:119], v[152:159], v[168:175], v[116:119]
	v_mfma_f32_16x16x128_f8f6f4 v[112:115], v[160:167], v[168:175], v[112:115]
	v_mfma_f32_16x16x128_f8f6f4 v[100:103], v[152:159], v[198:205], v[100:103]
	v_mfma_f32_16x16x128_f8f6f4 v[96:99], v[160:167], v[198:205], v[96:99]
	v_mfma_f32_16x16x128_f8f6f4 v[168:171], v[152:159], v[206:213], v[84:87]
	v_mfma_f32_16x16x128_f8f6f4 v[172:175], v[160:167], v[206:213], v[80:83]
	v_mfma_f32_16x16x128_f8f6f4 v[194:197], v[152:159], v[214:221], v[68:71]
	v_mfma_f32_16x16x128_f8f6f4 v[198:201], v[160:167], v[214:221], v[64:67]
	s_setprio 0
	s_barrier
	s_mov_b32 m0, s62
	s_nop 3
	ds_read_b128 v[64:67], v135 offset:16384
	ds_read_b128 v[68:71], v135 offset:17408
	ds_read_b128 v[72:75], v135 offset:18432
	ds_read_b128 v[76:79], v135 offset:19456
	ds_read_b128 v[80:83], v135 offset:20480
	ds_read_b128 v[84:87], v135 offset:21504
	ds_read_b128 v[88:91], v135 offset:22528
	ds_read_b128 v[92:95], v135 offset:23552
	buffer_load_dwordx4 v130, s[48:51], s31 offen lds
	s_mov_b32 m0, s63
	s_add_i32 s38, s31, 0xb0000
	buffer_load_dwordx4 v131, s[48:51], s31 offen lds
	s_mov_b32 m0, s64
	s_nop 0
	buffer_load_dwordx4 v130, s[48:51], s38 offen lds
	s_mov_b32 m0, s65
	s_nop 0
	buffer_load_dwordx4 v131, s[48:51], s38 offen lds
	s_mov_b32 m0, s61
	s_nop 0
	buffer_load_dwordx4 v132, s[44:47], s31 offen lds
	s_mov_b32 m0, s66
	s_nop 0
	buffer_load_dwordx4 v133, s[44:47], s31 offen lds
	s_waitcnt vmcnt(8)
	s_waitcnt lgkmcnt(0)
	s_barrier
	s_setprio 1
	s_waitcnt lgkmcnt(6)
	v_mfma_f32_16x16x128_f8f6f4 v[60:63], v[136:143], v[64:71], v[60:63]
	v_mfma_f32_16x16x128_f8f6f4 v[0:3], v[144:151], v[64:71], v[0:3]
	s_waitcnt lgkmcnt(4)
	v_mfma_f32_16x16x128_f8f6f4 v[202:205], v[136:143], v[72:79], v[48:51]
	v_mfma_f32_16x16x128_f8f6f4 v[206:209], v[144:151], v[72:79], v[44:47]
	s_waitcnt lgkmcnt(2)
	v_mfma_f32_16x16x128_f8f6f4 v[210:213], v[136:143], v[80:87], v[32:35]
	v_mfma_f32_16x16x128_f8f6f4 v[214:217], v[144:151], v[80:87], v[28:31]
	s_waitcnt lgkmcnt(0)
	v_mfma_f32_16x16x128_f8f6f4 v[218:221], v[136:143], v[88:95], v[16:19]
	v_mfma_f32_16x16x128_f8f6f4 v[222:225], v[144:151], v[88:95], v[12:15]
	s_setprio 0
	s_setprio 1
	v_mfma_f32_16x16x128_f8f6f4 v[56:59], v[152:159], v[64:71], v[56:59]
	v_mfma_f32_16x16x128_f8f6f4 v[52:55], v[160:167], v[64:71], v[52:55]
	v_mfma_f32_16x16x128_f8f6f4 v[226:229], v[152:159], v[72:79], v[40:43]
	v_mfma_f32_16x16x128_f8f6f4 v[232:235], v[160:167], v[72:79], v[36:39]
	v_mfma_f32_16x16x128_f8f6f4 v[236:239], v[152:159], v[80:87], v[24:27]
	v_mfma_f32_16x16x128_f8f6f4 v[240:243], v[160:167], v[80:87], v[20:23]
	v_mfma_f32_16x16x128_f8f6f4 v[244:247], v[152:159], v[88:95], v[8:11]
	v_mfma_f32_16x16x128_f8f6f4 v[248:251], v[160:167], v[88:95], v[4:7]
	s_setprio 0
	s_barrier
	v_add_u32_e32 v12, 0x18000, v134
	s_nop 3
	ds_read_b128 v[4:7], v12
	ds_read_b128 v[8:11], v12 offset:1024
	ds_read_b128 v[20:23], v12 offset:2048
	ds_read_b128 v[24:27], v12 offset:3072
	v_add_u32_e32 v12, 0x1c000, v134
	ds_read_b128 v[136:139], v12
	ds_read_b128 v[140:143], v12 offset:1024
	ds_read_b128 v[144:147], v12 offset:2048
	ds_read_b128 v[148:151], v12 offset:3072
	s_mov_b32 m0, s67
	ds_read_b128 v[12:15], v135 offset:32768
	ds_read_b128 v[16:19], v135 offset:33792
	ds_read_b128 v[28:31], v135 offset:34816
	ds_read_b128 v[32:35], v135 offset:35840
	ds_read_b128 v[36:39], v135 offset:36864
	ds_read_b128 v[40:43], v135 offset:37888
	ds_read_b128 v[44:47], v135 offset:38912
	ds_read_b128 v[48:51], v135 offset:39936
	buffer_load_dwordx4 v132, s[44:47], s38 offen lds
	s_mov_b32 m0, s68
	s_nop 0
	buffer_load_dwordx4 v133, s[44:47], s38 offen lds
	s_waitcnt vmcnt(8)
	s_waitcnt lgkmcnt(0)
	s_barrier
	s_setprio 1
	s_waitcnt lgkmcnt(6)
	v_mfma_f32_16x16x128_f8f6f4 v[124:127], v[4:11], v[12:19], v[124:127]
	v_mfma_f32_16x16x128_f8f6f4 v[120:123], v[20:27], v[12:19], v[120:123]
	s_waitcnt lgkmcnt(4)
	v_mfma_f32_16x16x128_f8f6f4 v[108:111], v[4:11], v[28:35], v[108:111]
	v_mfma_f32_16x16x128_f8f6f4 v[104:107], v[20:27], v[28:35], v[104:107]
	s_waitcnt lgkmcnt(2)
	v_mfma_f32_16x16x128_f8f6f4 v[92:95], v[4:11], v[36:43], v[178:181]
	v_mfma_f32_16x16x128_f8f6f4 v[88:91], v[20:27], v[36:43], v[182:185]
	s_waitcnt lgkmcnt(0)
	v_mfma_f32_16x16x128_f8f6f4 v[76:79], v[4:11], v[44:51], v[186:189]
	v_mfma_f32_16x16x128_f8f6f4 v[72:75], v[20:27], v[44:51], v[190:193]
	s_setprio 0
	s_setprio 1
	v_mfma_f32_16x16x128_f8f6f4 v[116:119], v[136:143], v[12:19], v[116:119]
	v_mfma_f32_16x16x128_f8f6f4 v[112:115], v[144:151], v[12:19], v[112:115]
	v_mfma_f32_16x16x128_f8f6f4 v[100:103], v[136:143], v[28:35], v[100:103]
	v_mfma_f32_16x16x128_f8f6f4 v[96:99], v[144:151], v[28:35], v[96:99]
	v_mfma_f32_16x16x128_f8f6f4 v[84:87], v[136:143], v[36:43], v[168:171]
	v_mfma_f32_16x16x128_f8f6f4 v[80:83], v[144:151], v[36:43], v[172:175]
	v_mfma_f32_16x16x128_f8f6f4 v[68:71], v[136:143], v[44:51], v[194:197]
	v_mfma_f32_16x16x128_f8f6f4 v[64:67], v[144:151], v[44:51], v[198:201]
	s_setprio 0
	s_barrier
	s_mov_b32 m0, s69
	s_or_b32 s38, s31, 0x80
	ds_read_b128 v[36:39], v135 offset:49152
	ds_read_b128 v[40:43], v135 offset:50176
	ds_read_b128 v[152:155], v135 offset:51200
	ds_read_b128 v[156:159], v135 offset:52224
	ds_read_b128 v[160:163], v135 offset:53248
	ds_read_b128 v[164:167], v135 offset:54272
	ds_read_b128 v[168:171], v135 offset:55296
	ds_read_b128 v[172:175], v135 offset:56320
	buffer_load_dwordx4 v130, s[48:51], s38 offen lds
	s_mov_b32 m0, s70
	s_add_i32 s31, s31, 0xb0080
	buffer_load_dwordx4 v131, s[48:51], s38 offen lds
	s_mov_b32 m0, s73
	s_nop 0
	buffer_load_dwordx4 v130, s[48:51], s31 offen lds
	s_mov_b32 m0, s74
	s_nop 0
	buffer_load_dwordx4 v131, s[48:51], s31 offen lds
	s_mov_b32 m0, s71
	s_nop 0
	buffer_load_dwordx4 v132, s[44:47], s38 offen lds
	s_mov_b32 m0, s72
	s_nop 0
	buffer_load_dwordx4 v133, s[44:47], s38 offen lds
	s_waitcnt vmcnt(8)
	s_waitcnt lgkmcnt(0)
	s_barrier
	s_setprio 1
	s_waitcnt lgkmcnt(6)
	v_mfma_f32_16x16x128_f8f6f4 v[60:63], v[4:11], v[36:43], v[60:63]
	v_mfma_f32_16x16x128_f8f6f4 v[0:3], v[20:27], v[36:43], v[0:3]
	s_waitcnt lgkmcnt(4)
	v_mfma_f32_16x16x128_f8f6f4 v[48:51], v[4:11], v[152:159], v[202:205]
	v_mfma_f32_16x16x128_f8f6f4 v[44:47], v[20:27], v[152:159], v[206:209]
	s_waitcnt lgkmcnt(2)
	v_mfma_f32_16x16x128_f8f6f4 v[32:35], v[4:11], v[160:167], v[210:213]
	v_mfma_f32_16x16x128_f8f6f4 v[28:31], v[20:27], v[160:167], v[214:217]
	s_waitcnt lgkmcnt(0)
	v_mfma_f32_16x16x128_f8f6f4 v[16:19], v[4:11], v[168:175], v[218:221]
	v_mfma_f32_16x16x128_f8f6f4 v[12:15], v[20:27], v[168:175], v[222:225]
	s_setprio 0
	s_setprio 1
	v_mfma_f32_16x16x128_f8f6f4 v[56:59], v[136:143], v[36:43], v[56:59]
	v_mfma_f32_16x16x128_f8f6f4 v[52:55], v[144:151], v[36:43], v[52:55]
	v_mfma_f32_16x16x128_f8f6f4 v[40:43], v[136:143], v[152:159], v[226:229]
	v_mfma_f32_16x16x128_f8f6f4 v[36:39], v[144:151], v[152:159], v[232:235]
	v_mfma_f32_16x16x128_f8f6f4 v[24:27], v[136:143], v[160:167], v[236:239]
	v_mfma_f32_16x16x128_f8f6f4 v[20:23], v[144:151], v[160:167], v[240:243]
	v_mfma_f32_16x16x128_f8f6f4 v[8:11], v[136:143], v[168:175], v[244:247]
	v_mfma_f32_16x16x128_f8f6f4 v[4:7], v[144:151], v[168:175], v[248:251]
	s_setprio 0
	s_barrier
	s_add_i32 s12, s12, 2
	s_addk_i32 s13, 0x100
	s_cmp_gt_u32 s12, 41
	s_cbranch_scc0 .LBB0_1825
	s_and_b64 vcc, exec, s[8:9]
	s_cbranch_vccz .LBB0_1828
	s_barrier
